# code placement: untouched loops back at their baseline offsets (padding behind rewritten regions)
# speedup vs baseline: 1.0217x; 1.0030x over previous
.LBB0_438:
	v_cvt_f32_u32_e32 v34, s83
	s_sub_i32 s54, 0, s83
	s_abs_i32 s7, s81
	s_ashr_i32 s6, s81, 31
	v_rcp_iflag_f32_e32 v34, v34
	s_nop 0
	v_mul_f32_e32 v34, 0x4f7ffffe, v34
	v_cvt_u32_f32_e32 v34, v34
	s_nop 0
	v_readfirstlane_b32 s55, v34
	s_mul_i32 s54, s54, s55
	s_mul_hi_u32 s54, s55, s54
	s_add_i32 s55, s55, s54
	s_mul_hi_u32 s54, s7, s55
	s_mul_i32 s55, s54, s83
	s_sub_i32 s7, s7, s55
	s_add_i32 s56, s54, 1
	s_sub_i32 s55, s7, s83
	s_cmp_ge_u32 s7, s83
	s_cselect_b32 s54, s56, s54
	s_cselect_b32 s7, s55, s7
	s_add_i32 s55, s54, 1
	s_cmp_ge_u32 s7, s83
	s_cselect_b32 s7, s55, s54
	s_xor_b32 s7, s7, s6
	s_sub_i32 s6, s7, s6
	s_mul_i32 s7, s6, s83
	s_lshl_b32 s6, s6, 6
	s_sub_i32 s7, s81, s7
	s_add_i32 s54, s26, -1
	v_or_b32_e32 v35, s6, v84
	s_ashr_i32 s6, s6, 31
	v_lshl_or_b32 v34, s7, 5, v1
	v_min_i32_e32 v34, s54, v34
	s_mul_i32 s54, s6, s26
	v_mad_u64_u32 v[36:37], s[6:7], v35, s26, 0
	v_add_u32_e32 v37, s54, v37
	s_waitcnt lgkmcnt(0)
	v_lshl_add_u64 v[36:37], v[36:37], 2, s[4:5]
	v_ashrrev_i32_e32 v35, 31, v34
	v_lshl_add_u64 v[34:35], v[34:35], 2, v[36:37]
	s_lshl_b64 s[4:5], s[26:27], 3
	v_lshl_add_u64 v[36:37], v[34:35], 0, s[4:5]
	v_lshl_add_u64 v[38:39], v[36:37], 0, s[4:5]
	v_lshl_add_u64 v[40:41], v[38:39], 0, s[4:5]
	v_lshl_add_u64 v[42:43], v[40:41], 0, s[4:5]
	v_lshl_add_u64 v[44:45], v[42:43], 0, s[4:5]
	v_lshl_add_u64 v[46:47], v[44:45], 0, s[4:5]
	v_lshl_add_u64 v[48:49], v[46:47], 0, s[4:5]
	global_load_dword v34, v[34:35], off nt
	s_nop 0
	global_load_dword v35, v[36:37], off nt
	s_nop 0
	global_load_dword v36, v[38:39], off nt
	global_load_dword v37, v[40:41], off nt
	s_nop 0
	global_load_dword v38, v[42:43], off nt
	global_load_dword v39, v[44:45], off nt
	global_load_dword v40, v[46:47], off nt
	global_load_dword v41, v[48:49], off nt
	v_lshl_add_u64 v[44:45], v[48:49], 0, s[4:5]
	global_load_dword v42, v[44:45], off nt
	v_lshl_add_u64 v[44:45], v[44:45], 0, s[4:5]
	v_lshl_add_u64 v[46:47], v[44:45], 0, s[4:5]
	global_load_dword v43, v[44:45], off nt
	s_nop 0
	global_load_dword v44, v[46:47], off nt
	v_lshl_add_u64 v[46:47], v[46:47], 0, s[4:5]
	v_lshl_add_u64 v[48:49], v[46:47], 0, s[4:5]
	global_load_dword v45, v[46:47], off nt
	s_nop 0
	global_load_dword v46, v[48:49], off nt
	v_lshl_add_u64 v[48:49], v[48:49], 0, s[4:5]
	v_lshl_add_u64 v[50:51], v[48:49], 0, s[4:5]
	global_load_dword v47, v[48:49], off nt
	s_nop 0
	global_load_dword v48, v[50:51], off nt
	v_lshl_add_u64 v[50:51], v[50:51], 0, s[4:5]
	v_lshl_add_u64 v[52:53], v[50:51], 0, s[4:5]
	global_load_dword v49, v[50:51], off nt
	s_nop 0
	global_load_dword v50, v[52:53], off nt
	v_lshl_add_u64 v[52:53], v[52:53], 0, s[4:5]
	v_lshl_add_u64 v[54:55], v[52:53], 0, s[4:5]
	global_load_dword v51, v[52:53], off nt
	s_nop 0
	global_load_dword v52, v[54:55], off nt
	v_lshl_add_u64 v[54:55], v[54:55], 0, s[4:5]
	v_lshl_add_u64 v[56:57], v[54:55], 0, s[4:5]
	global_load_dword v53, v[54:55], off nt
	s_nop 0
	global_load_dword v54, v[56:57], off nt
	v_lshl_add_u64 v[56:57], v[56:57], 0, s[4:5]
	v_lshl_add_u64 v[58:59], v[56:57], 0, s[4:5]
	global_load_dword v55, v[56:57], off nt
	s_nop 0
	global_load_dword v56, v[58:59], off nt
	v_lshl_add_u64 v[58:59], v[58:59], 0, s[4:5]
	v_lshl_add_u64 v[60:61], v[58:59], 0, s[4:5]
	global_load_dword v57, v[58:59], off nt
	s_nop 0
	global_load_dword v58, v[60:61], off nt
	v_lshl_add_u64 v[60:61], v[60:61], 0, s[4:5]
	v_lshl_add_u64 v[62:63], v[60:61], 0, s[4:5]
	global_load_dword v59, v[60:61], off nt
	s_nop 0
	global_load_dword v60, v[62:63], off nt
	v_lshl_add_u64 v[62:63], v[62:63], 0, s[4:5]
	v_lshl_add_u64 v[64:65], v[62:63], 0, s[4:5]
	global_load_dword v61, v[62:63], off nt
	s_nop 0
	global_load_dword v62, v[64:65], off nt
	v_lshl_add_u64 v[64:65], v[64:65], 0, s[4:5]
	v_lshl_add_u64 v[68:69], v[64:65], 0, s[4:5]
	global_load_dword v63, v[64:65], off nt
	s_nop 0
	global_load_dword v64, v[68:69], off nt
	v_lshl_add_u64 v[68:69], v[68:69], 0, s[4:5]
	global_load_dword v65, v[68:69], off nt
	s_abs_i32 s4, s3
	v_cvt_f32_u32_e32 v68, s4
	s_sub_i32 s7, 0, s4
	s_abs_i32 s6, s2
	s_xor_b32 s5, s2, s3
	v_rcp_iflag_f32_e32 v68, v68
	s_ashr_i32 s5, s5, 31
	s_waitcnt vmcnt(62)
	ds_write2_b32 v94, v2, v3 offset1:66
	s_waitcnt vmcnt(60)
	ds_write2_b32 v94, v4, v5 offset0:132 offset1:198
	v_mul_f32_e32 v68, 0x4f7ffffe, v68
	v_cvt_u32_f32_e32 v68, v68
	s_nop 0
	v_readfirstlane_b32 s54, v68
	s_mul_i32 s7, s7, s54
	s_mul_hi_u32 s7, s54, s7
	s_add_i32 s54, s54, s7
	s_mul_hi_u32 s7, s6, s54
	s_mul_i32 s54, s7, s4
	s_sub_i32 s6, s6, s54
	s_add_i32 s55, s7, 1
	s_sub_i32 s54, s6, s4
	s_cmp_ge_u32 s6, s4
	v_add_u32_e32 v68, 0x400, v94
	s_cselect_b32 s7, s55, s7
	s_waitcnt vmcnt(58)
	ds_write2_b32 v68, v6, v7 offset0:8 offset1:74
	s_waitcnt vmcnt(56)
	ds_write2_b32 v68, v8, v9 offset0:140 offset1:206
	v_add_u32_e32 v68, 0x800, v94
	s_cselect_b32 s6, s54, s6
	s_add_i32 s54, s7, 1
	s_waitcnt vmcnt(54)
	ds_write2_b32 v68, v10, v11 offset0:16 offset1:82
	s_waitcnt vmcnt(52)
	ds_write2_b32 v68, v12, v13 offset0:148 offset1:214
	v_add_u32_e32 v68, 0xc00, v94
	s_cmp_ge_u32 s6, s4
	s_waitcnt vmcnt(50)
	ds_write2_b32 v68, v14, v15 offset0:24 offset1:90
	s_waitcnt vmcnt(48)
	ds_write2_b32 v68, v16, v17 offset0:156 offset1:222
	v_add_u32_e32 v68, 0x1000, v94
	s_cselect_b32 s4, s54, s7
	s_waitcnt vmcnt(46)
	ds_write2_b32 v68, v18, v19 offset0:32 offset1:98
	s_waitcnt vmcnt(44)
	ds_write2_b32 v68, v20, v21 offset0:164 offset1:230
	v_add_u32_e32 v68, 0x1400, v94
	s_xor_b32 s4, s4, s5
	s_waitcnt vmcnt(42)
	ds_write2_b32 v68, v22, v23 offset0:40 offset1:106
	s_waitcnt vmcnt(40)
	ds_write2_b32 v68, v24, v25 offset0:172 offset1:238
	v_add_u32_e32 v68, 0x1800, v94
	s_sub_i32 s4, s4, s5
	s_waitcnt vmcnt(38)
	ds_write2_b32 v68, v26, v27 offset0:48 offset1:114
	s_waitcnt vmcnt(36)
	ds_write2_b32 v68, v28, v29 offset0:180 offset1:246
	v_add_u32_e32 v68, 0x1c00, v94
	s_mul_i32 s5, s4, s3
	s_waitcnt vmcnt(34)
	ds_write2_b32 v68, v30, v31 offset0:56 offset1:122
	s_waitcnt vmcnt(32)
	ds_write2_b32 v68, v32, v33 offset0:188 offset1:254
	s_branch .Lcv_cont_439
	s_nop 0
	s_nop 0
	s_nop 0

.LBB0_811:
	v_cvt_f32_u32_e32 v34, s83
	s_sub_i32 s54, 0, s83
	s_abs_i32 s7, s81
	s_ashr_i32 s6, s81, 31
	v_rcp_iflag_f32_e32 v34, v34
	s_nop 0
	v_mul_f32_e32 v34, 0x4f7ffffe, v34
	v_cvt_u32_f32_e32 v34, v34
	s_nop 0
	v_readfirstlane_b32 s55, v34
	s_mul_i32 s54, s54, s55
	s_mul_hi_u32 s54, s55, s54
	s_add_i32 s55, s55, s54
	s_mul_hi_u32 s54, s7, s55
	s_mul_i32 s55, s54, s83
	s_sub_i32 s7, s7, s55
	s_add_i32 s56, s54, 1
	s_sub_i32 s55, s7, s83
	s_cmp_ge_u32 s7, s83
	s_cselect_b32 s54, s56, s54
	s_cselect_b32 s7, s55, s7
	s_add_i32 s55, s54, 1
	s_cmp_ge_u32 s7, s83
	s_cselect_b32 s7, s55, s54
	s_xor_b32 s7, s7, s6
	s_sub_i32 s6, s7, s6
	s_mul_i32 s7, s6, s83
	s_lshl_b32 s6, s6, 6
	s_sub_i32 s7, s81, s7
	s_add_i32 s54, s26, -1
	v_or_b32_e32 v35, s6, v84
	s_ashr_i32 s6, s6, 31
	v_lshl_or_b32 v34, s7, 5, v1
	v_min_i32_e32 v34, s54, v34
	s_mul_i32 s54, s6, s26
	v_mad_u64_u32 v[36:37], s[6:7], v35, s26, 0
	v_add_u32_e32 v37, s54, v37
	s_waitcnt lgkmcnt(0)
	v_lshl_add_u64 v[36:37], v[36:37], 2, s[4:5]
	v_ashrrev_i32_e32 v35, 31, v34
	v_lshl_add_u64 v[34:35], v[34:35], 2, v[36:37]
	s_lshl_b64 s[4:5], s[26:27], 3
	v_lshl_add_u64 v[36:37], v[34:35], 0, s[4:5]
	v_lshl_add_u64 v[38:39], v[36:37], 0, s[4:5]
	v_lshl_add_u64 v[40:41], v[38:39], 0, s[4:5]
	v_lshl_add_u64 v[42:43], v[40:41], 0, s[4:5]
	v_lshl_add_u64 v[44:45], v[42:43], 0, s[4:5]
	v_lshl_add_u64 v[46:47], v[44:45], 0, s[4:5]
	v_lshl_add_u64 v[48:49], v[46:47], 0, s[4:5]
	global_load_dword v34, v[34:35], off nt
	s_nop 0
	global_load_dword v35, v[36:37], off nt
	s_nop 0
	global_load_dword v36, v[38:39], off nt
	global_load_dword v37, v[40:41], off nt
	s_nop 0
	global_load_dword v38, v[42:43], off nt
	global_load_dword v39, v[44:45], off nt
	global_load_dword v40, v[46:47], off nt
	global_load_dword v41, v[48:49], off nt
	v_lshl_add_u64 v[44:45], v[48:49], 0, s[4:5]
	global_load_dword v42, v[44:45], off nt
	v_lshl_add_u64 v[44:45], v[44:45], 0, s[4:5]
	v_lshl_add_u64 v[46:47], v[44:45], 0, s[4:5]
	global_load_dword v43, v[44:45], off nt
	s_nop 0
	global_load_dword v44, v[46:47], off nt
	v_lshl_add_u64 v[46:47], v[46:47], 0, s[4:5]
	v_lshl_add_u64 v[48:49], v[46:47], 0, s[4:5]
	global_load_dword v45, v[46:47], off nt
	s_nop 0
	global_load_dword v46, v[48:49], off nt
	v_lshl_add_u64 v[48:49], v[48:49], 0, s[4:5]
	v_lshl_add_u64 v[50:51], v[48:49], 0, s[4:5]
	global_load_dword v47, v[48:49], off nt
	s_nop 0
	global_load_dword v48, v[50:51], off nt
	v_lshl_add_u64 v[50:51], v[50:51], 0, s[4:5]
	v_lshl_add_u64 v[52:53], v[50:51], 0, s[4:5]
	global_load_dword v49, v[50:51], off nt
	s_nop 0
	global_load_dword v50, v[52:53], off nt
	v_lshl_add_u64 v[52:53], v[52:53], 0, s[4:5]
	v_lshl_add_u64 v[54:55], v[52:53], 0, s[4:5]
	global_load_dword v51, v[52:53], off nt
	s_nop 0
	global_load_dword v52, v[54:55], off nt
	v_lshl_add_u64 v[54:55], v[54:55], 0, s[4:5]
	v_lshl_add_u64 v[56:57], v[54:55], 0, s[4:5]
	global_load_dword v53, v[54:55], off nt
	s_nop 0
	global_load_dword v54, v[56:57], off nt
	v_lshl_add_u64 v[56:57], v[56:57], 0, s[4:5]
	v_lshl_add_u64 v[58:59], v[56:57], 0, s[4:5]
	global_load_dword v55, v[56:57], off nt
	s_nop 0
	global_load_dword v56, v[58:59], off nt
	v_lshl_add_u64 v[58:59], v[58:59], 0, s[4:5]
	v_lshl_add_u64 v[60:61], v[58:59], 0, s[4:5]
	global_load_dword v57, v[58:59], off nt
	s_nop 0
	global_load_dword v58, v[60:61], off nt
	v_lshl_add_u64 v[60:61], v[60:61], 0, s[4:5]
	v_lshl_add_u64 v[62:63], v[60:61], 0, s[4:5]
	global_load_dword v59, v[60:61], off nt
	s_nop 0
	global_load_dword v60, v[62:63], off nt
	v_lshl_add_u64 v[62:63], v[62:63], 0, s[4:5]
	v_lshl_add_u64 v[64:65], v[62:63], 0, s[4:5]
	global_load_dword v61, v[62:63], off nt
	s_nop 0
	global_load_dword v62, v[64:65], off nt
	v_lshl_add_u64 v[64:65], v[64:65], 0, s[4:5]
	v_lshl_add_u64 v[68:69], v[64:65], 0, s[4:5]
	global_load_dword v63, v[64:65], off nt
	s_nop 0
	global_load_dword v64, v[68:69], off nt
	v_lshl_add_u64 v[68:69], v[68:69], 0, s[4:5]
	global_load_dword v65, v[68:69], off nt
	s_abs_i32 s4, s2
	v_cvt_f32_u32_e32 v68, s4
	s_sub_i32 s7, 0, s4
	s_abs_i32 s6, s1
	s_xor_b32 s5, s1, s2
	v_rcp_iflag_f32_e32 v68, v68
	s_ashr_i32 s5, s5, 31
	s_waitcnt vmcnt(62)
	ds_write2_b32 v94, v2, v3 offset1:66
	s_waitcnt vmcnt(60)
	ds_write2_b32 v94, v4, v5 offset0:132 offset1:198
	v_mul_f32_e32 v68, 0x4f7ffffe, v68
	v_cvt_u32_f32_e32 v68, v68
	s_nop 0
	v_readfirstlane_b32 s54, v68
	s_mul_i32 s7, s7, s54
	s_mul_hi_u32 s7, s54, s7
	s_add_i32 s54, s54, s7
	s_mul_hi_u32 s7, s6, s54
	s_mul_i32 s54, s7, s4
	s_sub_i32 s6, s6, s54
	s_add_i32 s55, s7, 1
	s_sub_i32 s54, s6, s4
	s_cmp_ge_u32 s6, s4
	v_add_u32_e32 v68, 0x400, v94
	s_cselect_b32 s7, s55, s7
	s_waitcnt vmcnt(58)
	ds_write2_b32 v68, v6, v7 offset0:8 offset1:74
	s_waitcnt vmcnt(56)
	ds_write2_b32 v68, v8, v9 offset0:140 offset1:206
	v_add_u32_e32 v68, 0x800, v94
	s_cselect_b32 s6, s54, s6
	s_add_i32 s54, s7, 1
	s_waitcnt vmcnt(54)
	ds_write2_b32 v68, v10, v11 offset0:16 offset1:82
	s_waitcnt vmcnt(52)
	ds_write2_b32 v68, v12, v13 offset0:148 offset1:214
	v_add_u32_e32 v68, 0xc00, v94
	s_cmp_ge_u32 s6, s4
	s_waitcnt vmcnt(50)
	ds_write2_b32 v68, v14, v15 offset0:24 offset1:90
	s_waitcnt vmcnt(48)
	ds_write2_b32 v68, v16, v17 offset0:156 offset1:222
	v_add_u32_e32 v68, 0x1000, v94
	s_cselect_b32 s4, s54, s7
	s_waitcnt vmcnt(46)
	ds_write2_b32 v68, v18, v19 offset0:32 offset1:98
	s_waitcnt vmcnt(44)
	ds_write2_b32 v68, v20, v21 offset0:164 offset1:230
	v_add_u32_e32 v68, 0x1400, v94
	s_xor_b32 s4, s4, s5
	s_waitcnt vmcnt(42)
	ds_write2_b32 v68, v22, v23 offset0:40 offset1:106
	s_waitcnt vmcnt(40)
	ds_write2_b32 v68, v24, v25 offset0:172 offset1:238
	v_add_u32_e32 v68, 0x1800, v94
	s_sub_i32 s4, s4, s5
	s_waitcnt vmcnt(38)
	ds_write2_b32 v68, v26, v27 offset0:48 offset1:114
	s_waitcnt vmcnt(36)
	ds_write2_b32 v68, v28, v29 offset0:180 offset1:246
	v_add_u32_e32 v68, 0x1c00, v94
	s_mul_i32 s5, s4, s2
	s_waitcnt vmcnt(34)
	ds_write2_b32 v68, v30, v31 offset0:56 offset1:122
	s_waitcnt vmcnt(32)
	ds_write2_b32 v68, v32, v33 offset0:188 offset1:254
	s_branch .Lcv_cont_812
	s_nop 0
	s_nop 0
	s_nop 0

.Lcvda_go:
	v_add_u32_e32 v89, s72, v84
	v_add_u32_e32 v90, 1040, v89
	ds_read2_b32 v[4:5], v89 offset0:0 offset1:32
	ds_read2_b32 v[6:7], v89 offset0:64 offset1:96
	ds_read2_b32 v[8:9], v89 offset0:128 offset1:160
	ds_read2_b32 v[10:11], v89 offset0:192 offset1:224
	ds_read2_b32 v[12:13], v90 offset0:0 offset1:32
	ds_read2_b32 v[14:15], v90 offset0:64 offset1:96
	ds_read2_b32 v[16:17], v90 offset0:128 offset1:160
	ds_read2_b32 v[18:19], v90 offset0:192 offset1:224
	ds_read2_b32 v[20:21], v89 offset0:16 offset1:48
	ds_read2_b32 v[22:23], v89 offset0:80 offset1:112
	ds_read2_b32 v[24:25], v89 offset0:144 offset1:176
	ds_read2_b32 v[26:27], v89 offset0:208 offset1:240
	ds_read2_b32 v[28:29], v90 offset0:16 offset1:48
	ds_read2_b32 v[30:31], v90 offset0:80 offset1:112
	ds_read2_b32 v[32:33], v90 offset0:144 offset1:176
	ds_read2_b32 v[34:35], v90 offset0:208 offset1:240
	s_cmp_eq_u32 s98, 0
	s_cselect_b64 vcc, -1, 0
	s_movk_i32 s7, 0x2000
	s_cselect_b32 s7, 0x8000, s7
	v_cndmask_b32_e32 v91, v87, v86, vcc
	s_waitcnt lgkmcnt(8)
	v_pk_mul_f32 v[4:5], v[4:5], v[100:101]
	v_pk_mul_f32 v[6:7], v[6:7], v[100:101]
	v_pk_mul_f32 v[8:9], v[8:9], v[100:101]
	v_pk_mul_f32 v[10:11], v[10:11], v[100:101]
	v_pk_mul_f32 v[12:13], v[12:13], v[100:101]
	v_pk_mul_f32 v[14:15], v[14:15], v[100:101]
	v_pk_mul_f32 v[16:17], v[16:17], v[100:101]
	v_pk_mul_f32 v[18:19], v[18:19], v[100:101]
	v_cvt_pk_fp8_f32 v92, v4, v5
	v_cvt_pk_fp8_f32 v93, v8, v9
	v_cvt_pk_fp8_f32 v94, v12, v13
	v_cvt_pk_fp8_f32 v95, v16, v17
	v_cvt_pk_fp8_f32 v92, v6, v7 op_sel:[0,0,1]
	v_cvt_pk_fp8_f32 v93, v10, v11 op_sel:[0,0,1]
	v_cvt_pk_fp8_f32 v94, v14, v15 op_sel:[0,0,1]
	v_cvt_pk_fp8_f32 v95, v18, v19 op_sel:[0,0,1]
	global_store_dwordx4 v91, v[92:95], s[84:85] nt
	s_waitcnt lgkmcnt(0)
	v_pk_mul_f32 v[20:21], v[20:21], v[100:101]
	v_pk_mul_f32 v[22:23], v[22:23], v[100:101]
	v_pk_mul_f32 v[24:25], v[24:25], v[100:101]
	v_pk_mul_f32 v[26:27], v[26:27], v[100:101]
	v_pk_mul_f32 v[28:29], v[28:29], v[100:101]
	v_pk_mul_f32 v[30:31], v[30:31], v[100:101]
	v_pk_mul_f32 v[32:33], v[32:33], v[100:101]
	v_pk_mul_f32 v[34:35], v[34:35], v[100:101]
	v_cvt_pk_fp8_f32 v96, v20, v21
	v_cvt_pk_fp8_f32 v97, v24, v25
	v_cvt_pk_fp8_f32 v98, v28, v29
	v_cvt_pk_fp8_f32 v99, v32, v33
	v_cvt_pk_fp8_f32 v96, v22, v23 op_sel:[0,0,1]
	v_cvt_pk_fp8_f32 v97, v26, v27 op_sel:[0,0,1]
	v_cvt_pk_fp8_f32 v98, v30, v31 op_sel:[0,0,1]
	v_cvt_pk_fp8_f32 v99, v34, v35 op_sel:[0,0,1]
	s_add_u32 s84, s84, s7
	s_addc_u32 s85, s85, 0
	global_store_dwordx4 v91, v[96:99], s[84:85] nt
	s_mov_b32 s32, 1
	s_cmp_eq_u32 s13, 0
	s_cbranch_scc1 .LBB0_1759
	s_mov_b32 s25, s12
	s_mov_b32 s7, s72
	s_mov_b32 s72, s86
	s_mov_b32 s86, s7
	s_branch .Lcvda_loop
	s_nop 0
	s_nop 0

.LBB0_2419:
	s_lshl_b32 s2, s2, 13
	s_add_i32 s76, s2, 0
	s_add_i32 s76, s76, 0x10000
	s_andn2_b64 vcc, exec, s[8:9]
	v_lshlrev_b32_e32 v134, 2, v162
	s_cbranch_vccnz .LBB0_2468
	v_or_b32_e32 v6, 32, v168
	v_cmp_gt_i32_e64 s[40:41], v6, v2
	v_cmp_lt_i32_e64 s[42:43], v6, v2
	v_or_b32_e32 v6, 34, v168
	v_cmp_gt_i32_e64 s[44:45], v6, v2
	v_or_b32_e32 v6, 35, v168
	v_cmp_gt_i32_e64 s[46:47], v6, v2
	v_or_b32_e32 v6, 40, v168
	v_cmp_gt_i32_e64 s[48:49], v6, v2
	v_or_b32_e32 v6, 41, v168
	v_cmp_gt_i32_e64 s[50:51], v6, v2
	v_or_b32_e32 v6, 42, v168
	v_cmp_gt_i32_e64 s[52:53], v6, v2
	v_or_b32_e32 v6, 43, v168
	v_cmp_gt_i32_e64 s[54:55], v6, v2
	v_or_b32_e32 v6, 48, v168
	v_cmp_gt_i32_e64 s[56:57], v6, v2
	v_or_b32_e32 v6, 49, v168
	v_cmp_gt_i32_e64 s[58:59], v6, v2
	v_or_b32_e32 v6, 50, v168
	v_cmp_gt_i32_e64 s[60:61], v6, v2
	v_or_b32_e32 v6, 51, v168
	v_cmp_gt_i32_e64 s[62:63], v6, v2
	v_or_b32_e32 v6, 56, v168
	v_cmp_gt_i32_e64 s[64:65], v6, v2
	v_or_b32_e32 v6, 57, v168
	v_cmp_gt_i32_e64 s[66:67], v6, v2
	v_or_b32_e32 v6, 58, v168
	v_cmp_gt_i32_e64 s[68:69], v6, v2
	v_or_b32_e32 v6, 59, v168
	v_cmp_gt_i32_e64 s[6:7], v168, v2
	v_cmp_lt_i32_e64 s[8:9], v168, v2
	v_cmp_gt_i32_e64 s[10:11], v135, v2
	v_cmp_gt_i32_e64 s[12:13], v169, v2
	v_cmp_gt_i32_e64 s[14:15], v170, v2
	v_cmp_gt_i32_e64 s[16:17], v171, v2
	v_cmp_gt_i32_e64 s[18:19], v172, v2
	v_cmp_gt_i32_e64 s[20:21], v173, v2
	v_cmp_gt_i32_e64 s[22:23], v174, v2
	v_cmp_gt_i32_e64 s[24:25], v175, v2
	v_cmp_gt_i32_e64 s[26:27], v176, v2
	v_cmp_gt_i32_e64 s[28:29], v177, v2
	v_cmp_gt_i32_e64 s[30:31], v178, v2
	v_cmp_gt_i32_e64 s[34:35], v179, v2
	v_cmp_gt_i32_e64 s[36:37], v180, v2
	v_cmp_gt_i32_e64 s[38:39], v181, v2
	v_cmp_gt_i32_e64 s[70:71], v6, v2
	s_min_u32 s2, s92, 8
	v_lshlrev_b32_e32 v2, 4, v4
	s_add_i32 s2, s92, s2
	v_and_b32_e32 v2, 0xc0, v2
	s_lshl_b32 s87, s2, 13
	v_lshl_or_b32 v2, v160, 8, v2
	v_readlane_b32 s2, v247, 4
	v_lshlrev_b32_e32 v5, 1, v4
	v_mov_b32_e32 v140, 0
	v_add_u32_e32 v185, s2, v2
	v_readlane_b32 s2, v247, 5
	s_movk_i32 s96, 0xc00
	s_add_i32 s91, s91, s92
	v_add_u32_e32 v187, s2, v2
	v_readlane_b32 s2, v247, 6
	s_add_i32 s93, s93, s3
	v_mov_b32_e32 v139, v131
	v_add_u32_e32 v188, s2, v2
	v_readlane_b32 s2, v247, 7
	s_mov_b32 s94, 2
	v_add_u32_e32 v183, s75, v134
	v_add_u32_e32 v189, s2, v2
	v_readlane_b32 s2, v247, 8
	v_add3_u32 v184, s76, v166, v134
	s_lshl_b32 s95, s92, 13
	v_add_u32_e32 v190, s2, v2
	v_readlane_b32 s2, v247, 9
	s_addk_i32 s87, 0x4000
	v_and_or_b32 v186, v5, 32, v3
	v_add_u32_e32 v191, s2, v2
	v_readlane_b32 s2, v247, 10
	s_add_i32 s86, s75, 0xc000
	s_mov_b32 s3, 0
	v_add_u32_e32 v192, s2, v2
	v_readlane_b32 s2, v247, 11
	v_mov_b32_e32 v202, 0
	v_mov_b32_e32 v3, v140
	v_add_u32_e32 v193, s2, v2
	v_readlane_b32 s2, v247, 12
	v_mov_b32_e32 v4, v140
	v_mov_b32_e32 v5, v140
	v_add_u32_e32 v194, s2, v2
	v_readlane_b32 s2, v247, 13
	v_mov_b32_e32 v6, v140
	v_mov_b32_e32 v7, v140
	v_add_u32_e32 v195, s2, v2
	v_readlane_b32 s2, v247, 14
	v_mov_b32_e32 v8, v140
	v_mov_b32_e32 v9, v140
	v_add_u32_e32 v196, s2, v2
	v_readlane_b32 s2, v247, 15
	v_mov_b32_e32 v10, v140
	v_mov_b32_e32 v11, v140
	v_add_u32_e32 v197, s2, v2
	v_readlane_b32 s2, v247, 16
	v_mov_b32_e32 v12, v140
	v_mov_b32_e32 v13, v140
	v_add_u32_e32 v198, s2, v2
	v_readlane_b32 s2, v247, 17
	v_mov_b32_e32 v14, v140
	v_mov_b32_e32 v15, v140
	v_add_u32_e32 v199, s2, v2
	v_readlane_b32 s2, v247, 21
	v_mov_b32_e32 v16, v140
	v_mov_b32_e32 v17, v140
	v_add_u32_e32 v200, s2, v2
	s_add_i32 s2, 0, 0x8000
	v_add_u32_e32 v201, s2, v2
	s_mov_b32 s2, 0
	v_mov_b32_e32 v2, 0
	v_mov_b32_e32 v18, 0
	v_mov_b32_e32 v19, v140
	v_mov_b32_e32 v20, v140
	v_mov_b32_e32 v21, v140
	v_mov_b32_e32 v22, v140
	v_mov_b32_e32 v23, v140
	v_add_u32_e32 v226, v201, v186
	s_nop 0
	s_nop 0
	s_nop 0
	s_nop 0
	s_nop 0
	s_nop 0
	s_nop 0
	s_nop 0
	s_nop 0
	s_nop 0
	s_nop 0
	s_nop 0
	s_nop 0
	s_nop 0
	s_nop 0
	v_mov_b32_e32 v24, v140
	v_mov_b32_e32 v25, v140
	v_mov_b32_e32 v26, v140
	v_mov_b32_e32 v27, v140
	v_mov_b32_e32 v28, v140
	v_mov_b32_e32 v29, v140
	v_mov_b32_e32 v30, v140
	v_mov_b32_e32 v31, v140
	v_mov_b32_e32 v32, v140
	v_mov_b32_e32 v33, v140
	s_branch .LBB0_2422

.Lcvdc_go:
	v_add_u32_e32 v89, s72, v84
	v_add_u32_e32 v90, 1040, v89
	ds_read2_b32 v[4:5], v89 offset0:0 offset1:32
	ds_read2_b32 v[6:7], v89 offset0:64 offset1:96
	ds_read2_b32 v[8:9], v89 offset0:128 offset1:160
	ds_read2_b32 v[10:11], v89 offset0:192 offset1:224
	ds_read2_b32 v[12:13], v90 offset0:0 offset1:32
	ds_read2_b32 v[14:15], v90 offset0:64 offset1:96
	ds_read2_b32 v[16:17], v90 offset0:128 offset1:160
	ds_read2_b32 v[18:19], v90 offset0:192 offset1:224
	ds_read2_b32 v[20:21], v89 offset0:16 offset1:48
	ds_read2_b32 v[22:23], v89 offset0:80 offset1:112
	ds_read2_b32 v[24:25], v89 offset0:144 offset1:176
	ds_read2_b32 v[26:27], v89 offset0:208 offset1:240
	ds_read2_b32 v[28:29], v90 offset0:16 offset1:48
	ds_read2_b32 v[30:31], v90 offset0:80 offset1:112
	ds_read2_b32 v[32:33], v90 offset0:144 offset1:176
	ds_read2_b32 v[34:35], v90 offset0:208 offset1:240
	s_cmp_eq_u32 s98, 0
	s_cselect_b64 vcc, -1, 0
	s_movk_i32 s7, 0x2000
	s_cselect_b32 s7, 0x8000, s7
	v_cndmask_b32_e32 v91, v87, v86, vcc
	s_waitcnt lgkmcnt(8)
	v_pk_mul_f32 v[4:5], v[4:5], v[100:101]
	v_pk_mul_f32 v[6:7], v[6:7], v[100:101]
	v_pk_mul_f32 v[8:9], v[8:9], v[100:101]
	v_pk_mul_f32 v[10:11], v[10:11], v[100:101]
	v_pk_mul_f32 v[12:13], v[12:13], v[100:101]
	v_pk_mul_f32 v[14:15], v[14:15], v[100:101]
	v_pk_mul_f32 v[16:17], v[16:17], v[100:101]
	v_pk_mul_f32 v[18:19], v[18:19], v[100:101]
	v_cvt_pk_fp8_f32 v92, v4, v5
	v_cvt_pk_fp8_f32 v93, v8, v9
	v_cvt_pk_fp8_f32 v94, v12, v13
	v_cvt_pk_fp8_f32 v95, v16, v17
	v_cvt_pk_fp8_f32 v92, v6, v7 op_sel:[0,0,1]
	v_cvt_pk_fp8_f32 v93, v10, v11 op_sel:[0,0,1]
	v_cvt_pk_fp8_f32 v94, v14, v15 op_sel:[0,0,1]
	v_cvt_pk_fp8_f32 v95, v18, v19 op_sel:[0,0,1]
	global_store_dwordx4 v91, v[92:95], s[84:85] nt
	s_waitcnt lgkmcnt(0)
	v_pk_mul_f32 v[20:21], v[20:21], v[100:101]
	v_pk_mul_f32 v[22:23], v[22:23], v[100:101]
	v_pk_mul_f32 v[24:25], v[24:25], v[100:101]
	v_pk_mul_f32 v[26:27], v[26:27], v[100:101]
	v_pk_mul_f32 v[28:29], v[28:29], v[100:101]
	v_pk_mul_f32 v[30:31], v[30:31], v[100:101]
	v_pk_mul_f32 v[32:33], v[32:33], v[100:101]
	v_pk_mul_f32 v[34:35], v[34:35], v[100:101]
	v_cvt_pk_fp8_f32 v96, v20, v21
	v_cvt_pk_fp8_f32 v97, v24, v25
	v_cvt_pk_fp8_f32 v98, v28, v29
	v_cvt_pk_fp8_f32 v99, v32, v33
	v_cvt_pk_fp8_f32 v96, v22, v23 op_sel:[0,0,1]
	v_cvt_pk_fp8_f32 v97, v26, v27 op_sel:[0,0,1]
	v_cvt_pk_fp8_f32 v98, v30, v31 op_sel:[0,0,1]
	v_cvt_pk_fp8_f32 v99, v34, v35 op_sel:[0,0,1]
	s_add_u32 s84, s84, s7
	s_addc_u32 s85, s85, 0
	global_store_dwordx4 v91, v[96:99], s[84:85] nt
	s_mov_b32 s32, 1
	s_cmp_eq_u32 s13, 0
	s_cbranch_scc1 .LBB0_2858
	s_mov_b32 s25, s12
	s_mov_b32 s7, s72
	s_mov_b32 s72, s86
	s_mov_b32 s86, s7
	s_branch .Lcvdc_loop
	s_nop 0
	s_nop 0
	s_nop 0
	s_nop 0
	s_nop 0
	s_nop 0
	s_nop 0

.LBB0_4298:
	s_branch .LBB0_4275
	s_nop 0
	s_nop 0
	s_nop 0
	s_nop 0
	s_nop 0
	s_nop 0
	s_nop 0
